# speedup vs baseline: 1.0863x; 1.0863x over previous
.LBB5_83:
	s_or_b64 exec, exec, s[12:13]
	s_load_dwordx2 s[40:41], s[0:1], 0x78
	v_lshrrev_b32_e32 v126, 4, v128
	v_and_b32_e32 v127, 15, v0
	s_waitcnt vmcnt(12)
	v_mul_u32_u24_e32 v1, 48, v126
	s_waitcnt lgkmcnt(0)
	s_barrier
	v_or_b32_e32 v129, v1, v127
	s_mul_i32 s46, s45, 0xc00
	v_cmp_gt_u32_e64 s[2:3], 12, v127
	v_cndmask_b32_e64 v1, 0, 1, s[8:9]
	v_lshlrev_b32_e32 v131, 2, v126
	s_add_i32 s46, s46, 0x1b000
	v_mov_b32_e32 v71, 0
	v_cndmask_b32_e64 v130, 0, 1.0, s[2:3]
	v_cmp_ne_u32_e64 s[0:1], 1, v1
	s_andn2_b64 vcc, exec, s[8:9]
	v_add_u32_e32 v79, -8, v129
	v_mov_b32_e32 v70, 0
	s_cbranch_vccnz .Lmy_inact93
	v_cndmask_b32_e64 v1, v79, v129, s[2:3]
	v_lshlrev_b32_e32 v81, 2, v1
	v_add_u32_e32 v1, 0x22800, v81
	ds_read2_b32 v[6:7], v1 offset1:12
	ds_read2_b32 v[8:9], v1 offset0:24 offset1:36
	ds_read2_b32 v[10:11], v1 offset0:192 offset1:204
	ds_read2_b32 v[12:13], v1 offset0:216 offset1:228
	v_add_u32_e32 v2, 0x400, v1
	v_add_u32_e32 v1, 0x800, v1
	ds_read2_b32 v[14:15], v2 offset0:128 offset1:140
	ds_read2_b32 v[16:17], v2 offset0:152 offset1:164
	ds_read2_b32 v[70:71], v1 offset0:64 offset1:76
	ds_read_b128 v[2:5], v80
	ds_read2_b32 v[72:73], v1 offset0:88 offset1:100
	s_waitcnt lgkmcnt(0)
	v_cvt_pk_bf16_f32 v18, v6, v7
	v_cvt_pk_bf16_f32 v19, v8, v9
	ds_read_b128 v[6:9], v80 offset:1024
	v_cvt_pk_bf16_f32 v20, v10, v11
	v_cvt_pk_bf16_f32 v21, v12, v13
	ds_read_b128 v[10:13], v80 offset:2048
	v_cvt_pk_bf16_f32 v86, v14, v15
	v_mfma_f32_16x16x32_bf16 v[2:5], v[2:5], v[18:21], 0
	v_cvt_pk_bf16_f32 v87, v16, v17
	v_cvt_pk_bf16_f32 v88, v70, v71
	v_cvt_pk_bf16_f32 v89, v72, v73
	ds_read_b128 v[70:73], v80 offset:4096
	v_mov_b32_e32 v1, 0x23e00
	s_waitcnt lgkmcnt(2)
	v_mfma_f32_16x16x32_bf16 v[14:17], v[6:9], v[86:89], v[2:5]
	v_add_u32_e32 v96, s46, v81
	s_cmp_lt_i32 s48, 1
	ds_read_b128 v[74:77], v80 offset:6144
	ds_read_b128 v[2:5], v80 offset:3072
	s_waitcnt lgkmcnt(3)
	v_mfma_f32_16x16x32_bf16 v[6:9], v[10:13], v[18:21], 0
	s_mov_b32 s8, 0x43998000
	s_waitcnt lgkmcnt(0)
	v_mfma_f32_16x16x32_bf16 v[10:13], v[2:5], v[86:89], v[6:9]
	ds_read_b128 v[2:5], v80 offset:5120
	v_mfma_f32_16x16x32_bf16 v[6:9], v[70:73], v[18:21], 0
	ds_read_b128 v[70:73], v80 offset:7168
	s_waitcnt lgkmcnt(1)
	v_mfma_f32_16x16x32_bf16 v[6:9], v[2:5], v[86:89], v[6:9]
	v_mfma_f32_16x16x32_bf16 v[2:5], v[74:77], v[18:21], 0
	v_mov_b32_e32 v18, 0x23e10
	ds_read_b128 v[98:101], v1
	ds_read_b128 v[18:21], v18
	v_add_u32_e32 v1, s46, v80
	s_waitcnt vmcnt(11)
	ds_write_b128 v1, v[22:25]
	s_waitcnt vmcnt(10)
	ds_write_b128 v1, v[62:65] offset:1024
	s_waitcnt vmcnt(9)
	ds_write_b128 v1, v[66:69] offset:2048
	s_waitcnt lgkmcnt(5)
	v_mfma_f32_16x16x32_bf16 v[2:5], v[70:73], v[86:89], v[2:5]
	ds_read2_b32 v[88:89], v96 offset1:12
	ds_read2_b32 v[90:91], v96 offset0:24 offset1:36
	ds_read2_b32 v[86:87], v96 offset0:192 offset1:204
	ds_read2_b32 v[82:83], v96 offset0:216 offset1:228
	v_add_u32_e32 v63, 0x400, v96
	ds_read2_b32 v[66:67], v63 offset0:128 offset1:140
	ds_read2_b32 v[68:69], v63 offset0:152 offset1:164
	v_add_u32_e32 v62, 0x800, v96
	ds_read_b128 v[22:25], v80 offset:8192
	ds_read2_b32 v[94:95], v62 offset0:64 offset1:76
	ds_read2_b32 v[92:93], v62 offset0:88 offset1:100
	ds_read_b128 v[106:109], v80 offset:9216
	s_waitcnt lgkmcnt(9)
	v_cvt_pk_bf16_f32 v102, v88, v89
	s_waitcnt lgkmcnt(8)
	v_cvt_pk_bf16_f32 v103, v90, v91
	s_waitcnt lgkmcnt(7)
	v_cvt_pk_bf16_f32 v104, v86, v87
	s_waitcnt lgkmcnt(6)
	v_cvt_pk_bf16_f32 v105, v82, v83
	s_waitcnt lgkmcnt(5)
	v_cvt_pk_bf16_f32 v110, v66, v67
	s_waitcnt lgkmcnt(4)
	v_cvt_pk_bf16_f32 v111, v68, v69
	s_waitcnt lgkmcnt(3)
	v_mfma_f32_16x16x32_bf16 v[22:25], v[22:25], v[102:105], v[98:101]
	s_waitcnt lgkmcnt(2)
	v_cvt_pk_bf16_f32 v112, v94, v95
	s_waitcnt lgkmcnt(1)
	v_cvt_pk_bf16_f32 v113, v92, v93
	s_waitcnt lgkmcnt(0)
	s_nop 0
	v_mfma_f32_16x16x32_bf16 v[22:25], v[106:109], v[110:113], v[22:25]
	s_mul_i32 s58, s37, 0xc00
	v_add_u32_e32 v133, s58, v80
	global_load_dwordx4 v[136:139], v133, s[28:29]
	global_load_dwordx4 v[140:143], v133, s[28:29] offset:1024
	global_load_dwordx4 v[144:147], v133, s[28:29] offset:2048
	global_load_dwordx4 v[148:151], v133, s[30:31]
	global_load_dwordx4 v[156:159], v133, s[30:31] offset:1024
	global_load_dwordx4 v[160:163], v133, s[30:31] offset:2048
	s_cbranch_scc1 .LBB5_209
	s_waitcnt vmcnt(14)
	ds_write_b128 v1, v[50:53]
	s_waitcnt vmcnt(13)
	ds_write_b128 v1, v[54:57] offset:1024
	s_waitcnt vmcnt(12)
	ds_write_b128 v1, v[58:61] offset:2048
	ds_read2_b32 v[54:55], v96 offset1:12
	ds_read2_b32 v[56:57], v96 offset0:24 offset1:36
	ds_read2_b32 v[64:65], v96 offset0:192 offset1:204
	ds_read2_b32 v[98:99], v96 offset0:216 offset1:228
	ds_read2_b32 v[100:101], v63 offset0:128 offset1:140
	ds_read2_b32 v[102:103], v63 offset0:152 offset1:164
	ds_read2_b32 v[104:105], v62 offset0:64 offset1:76
	ds_read_b128 v[50:53], v80
	ds_read2_b32 v[106:107], v62 offset0:88 offset1:100
	ds_read_b128 v[58:61], v80 offset:1024
	s_waitcnt lgkmcnt(9)
	v_cvt_pk_bf16_f32 v54, v54, v55
	s_waitcnt lgkmcnt(8)
	v_cvt_pk_bf16_f32 v55, v56, v57
	s_waitcnt lgkmcnt(7)
	v_cvt_pk_bf16_f32 v56, v64, v65
	s_waitcnt lgkmcnt(6)
	v_cvt_pk_bf16_f32 v57, v98, v99
	s_waitcnt lgkmcnt(5)
	v_cvt_pk_bf16_f32 v62, v100, v101
	ds_read_b128 v[98:101], v80 offset:2048
	s_waitcnt lgkmcnt(3)
	v_mfma_f32_16x16x32_bf16 v[50:53], v[50:53], v[54:57], 0
	v_cvt_pk_bf16_f32 v63, v102, v103
	v_cvt_pk_bf16_f32 v64, v104, v105
	s_waitcnt lgkmcnt(2)
	v_cvt_pk_bf16_f32 v65, v106, v107
	s_waitcnt lgkmcnt(0)
	v_mfma_f32_16x16x32_bf16 v[98:101], v[98:101], v[54:57], 0
	ds_read_b128 v[102:105], v80 offset:4096
	ds_read_b128 v[106:109], v80 offset:11264
	v_mfma_f32_16x16x32_bf16 v[50:53], v[58:61], v[62:65], v[50:53]
	ds_read_b128 v[58:61], v80 offset:3072
	s_waitcnt lgkmcnt(0)
	v_mfma_f32_16x16x32_bf16 v[58:61], v[58:61], v[62:65], v[98:101]
	s_nop 2
	ds_read_b128 v[98:101], v80 offset:5120
	v_mfma_f32_16x16x32_bf16 v[102:105], v[102:105], v[54:57], 0
	s_waitcnt lgkmcnt(0)
	v_mfma_f32_16x16x32_bf16 v[98:101], v[98:101], v[62:65], v[102:105]
	s_nop 5
	ds_read_b128 v[102:105], v80 offset:10240
	v_mfma_f32_16x16x32_bf16 v[74:77], v[74:77], v[54:57], 0
	s_waitcnt lgkmcnt(0)
	v_mfma_f32_16x16x32_bf16 v[54:57], v[102:105], v[54:57], v[18:21]
	v_mfma_f32_16x16x32_bf16 v[54:57], v[106:109], v[62:65], v[54:57]
	v_mfma_f32_16x16x32_bf16 v[62:65], v[70:73], v[62:65], v[74:77]
	s_nop 6
	v_add_f32_e32 v54, v22, v54
	v_mul_f32_e32 v81, 0x3e4ccccd, v54
	v_cmp_lt_f32_e32 vcc, 0, v54
	v_add_f32_e32 v55, v23, v55
	v_mul_f32_e32 v97, 0x3e4ccccd, v55
	v_cndmask_b32_e32 v54, v81, v54, vcc
	v_cmp_lt_f32_e32 vcc, 0, v55
	v_mov_b32_e32 v81, s18
	v_fma_f32 v54, s15, v54, v81
	v_cndmask_b32_e32 v55, v97, v55, vcc
	v_fma_f32 v55, s15, v55, v81
	v_mul_f32_e32 v54, 0x3fb8aa3b, v54
	v_mul_f32_e32 v55, 0x3fb8aa3b, v55
	v_exp_f32_e32 v54, v54
	v_exp_f32_e32 v55, v55
	s_nop 0
	v_pk_add_f32 v[54:55], v[54:55], -1.0 op_sel_hi:[1,0]
	s_nop 0
	v_pk_fma_f32 v[16:17], v[52:53], v[54:55], v[16:17] op_sel_hi:[1,0,1]
	v_add_f32_e32 v52, v24, v56
	v_mul_f32_e32 v53, 0x3e4ccccd, v52
	v_cmp_lt_f32_e32 vcc, 0, v52
	v_pk_fma_f32 v[14:15], v[50:51], v[54:55], v[14:15] op_sel_hi:[1,0,1]
	v_pk_fma_f32 v[12:13], v[60:61], v[54:55], v[12:13] op_sel:[0,1,0]
	v_cndmask_b32_e32 v52, v53, v52, vcc
	v_add_f32_e32 v53, v25, v57
	v_mul_f32_e32 v56, 0x3e4ccccd, v53
	v_cmp_lt_f32_e32 vcc, 0, v53
	v_fma_f32 v52, s15, v52, v81
	v_mul_f32_e32 v52, 0x3fb8aa3b, v52
	v_cndmask_b32_e32 v53, v56, v53, vcc
	v_fma_f32 v53, s15, v53, v81
	v_mul_f32_e32 v53, 0x3fb8aa3b, v53
	v_exp_f32_e32 v52, v52
	v_exp_f32_e32 v53, v53
	v_pk_fma_f32 v[10:11], v[58:59], v[54:55], v[10:11] op_sel:[0,1,0]
	v_pk_add_f32 v[72:73], v[54:55], s[8:9] op_sel_hi:[1,0]
	v_pk_add_f32 v[50:51], v[52:53], -1.0 op_sel_hi:[1,0]
	s_nop 0
	v_pk_fma_f32 v[8:9], v[100:101], v[50:51], v[8:9] op_sel_hi:[1,0,1]
	v_pk_fma_f32 v[6:7], v[98:99], v[50:51], v[6:7] op_sel_hi:[1,0,1]
	v_pk_add_f32 v[70:71], v[50:51], s[8:9] op_sel_hi:[1,0]
	v_pk_fma_f32 v[4:5], v[64:65], v[50:51], v[4:5] op_sel:[0,1,0]
	v_pk_fma_f32 v[2:3], v[62:63], v[50:51], v[2:3] op_sel:[0,1,0]
	s_cmp_lt_i32 s48, 2
	s_cbranch_scc1 .LBB5_87
.LBB5_86:
	s_waitcnt vmcnt(11)
	ds_write_b128 v1, v[38:41]
	s_waitcnt vmcnt(10)
	ds_write_b128 v1, v[42:45] offset:1024
	s_waitcnt vmcnt(9)
	ds_write_b128 v1, v[46:49] offset:2048
	ds_read2_b32 v[42:43], v96 offset1:12
	ds_read2_b32 v[44:45], v96 offset0:24 offset1:36
	ds_read2_b32 v[50:51], v96 offset0:192 offset1:204
	ds_read2_b32 v[52:53], v96 offset0:216 offset1:228
	v_add_u32_e32 v38, 0x400, v96
	v_add_u32_e32 v46, 0x800, v96
	ds_read2_b32 v[54:55], v38 offset0:128 offset1:140
	ds_read2_b32 v[58:59], v38 offset0:152 offset1:164
	ds_read2_b32 v[60:61], v46 offset0:64 offset1:76
	ds_read_b128 v[38:41], v80
	ds_read2_b32 v[62:63], v46 offset0:88 offset1:100
	ds_read_b128 v[46:49], v80 offset:1024
	s_waitcnt lgkmcnt(9)
	v_cvt_pk_bf16_f32 v42, v42, v43
	s_waitcnt lgkmcnt(8)
	v_cvt_pk_bf16_f32 v43, v44, v45
	s_waitcnt lgkmcnt(7)
	v_cvt_pk_bf16_f32 v44, v50, v51
	s_waitcnt lgkmcnt(6)
	v_cvt_pk_bf16_f32 v45, v52, v53
	s_waitcnt lgkmcnt(5)
	v_cvt_pk_bf16_f32 v50, v54, v55
	ds_read_b128 v[54:57], v80 offset:2048
	s_waitcnt lgkmcnt(3)
	v_mfma_f32_16x16x32_bf16 v[38:41], v[38:41], v[42:45], 0
	v_cvt_pk_bf16_f32 v51, v58, v59
	v_cvt_pk_bf16_f32 v52, v60, v61
	s_waitcnt lgkmcnt(2)
	v_cvt_pk_bf16_f32 v53, v62, v63
	s_waitcnt lgkmcnt(0)
	v_mfma_f32_16x16x32_bf16 v[54:57], v[54:57], v[42:45], 0
	ds_read_b128 v[58:61], v80 offset:4096
	ds_read_b128 v[62:65], v80 offset:6144
	v_mfma_f32_16x16x32_bf16 v[38:41], v[46:49], v[50:53], v[38:41]
	ds_read_b128 v[46:49], v80 offset:3072
	s_waitcnt lgkmcnt(0)
	v_mfma_f32_16x16x32_bf16 v[46:49], v[46:49], v[50:53], v[54:57]
	s_nop 2
	ds_read_b128 v[54:57], v80 offset:5120
	v_mfma_f32_16x16x32_bf16 v[58:61], v[58:61], v[42:45], 0
	s_waitcnt lgkmcnt(0)
	v_mfma_f32_16x16x32_bf16 v[54:57], v[54:57], v[50:53], v[58:61]
	s_nop 5
	ds_read_b128 v[58:61], v80 offset:10240
	ds_read_b128 v[74:77], v80 offset:7168
	ds_read_b128 v[98:101], v80 offset:11264
	v_mfma_f32_16x16x32_bf16 v[62:65], v[62:65], v[42:45], 0
	s_waitcnt lgkmcnt(2)
	v_mfma_f32_16x16x32_bf16 v[42:45], v[58:61], v[42:45], v[18:21]
	s_waitcnt lgkmcnt(0)
	v_mfma_f32_16x16x32_bf16 v[42:45], v[98:101], v[50:53], v[42:45]
	v_mfma_f32_16x16x32_bf16 v[50:53], v[74:77], v[50:53], v[62:65]
	s_nop 6
	v_add_f32_e32 v42, v22, v42
	v_mul_f32_e32 v58, 0x3e4ccccd, v42
	v_cmp_lt_f32_e32 vcc, 0, v42
	v_add_f32_e32 v43, v23, v43
	v_mul_f32_e32 v59, 0x3e4ccccd, v43
	v_cndmask_b32_e32 v42, v58, v42, vcc
	v_cmp_lt_f32_e32 vcc, 0, v43
	v_mov_b32_e32 v58, s19
	v_fma_f32 v42, s16, v42, v58
	v_cndmask_b32_e32 v43, v59, v43, vcc
	v_fma_f32 v43, s16, v43, v58
	v_mul_f32_e32 v42, 0x3fb8aa3b, v42
	v_mul_f32_e32 v43, 0x3fb8aa3b, v43
	v_exp_f32_e32 v42, v42
	v_exp_f32_e32 v43, v43
	s_nop 0
	v_pk_add_f32 v[42:43], v[42:43], -1.0 op_sel_hi:[1,0]
	s_nop 0
	v_pk_fma_f32 v[16:17], v[40:41], v[42:43], v[16:17] op_sel_hi:[1,0,1]
	v_add_f32_e32 v40, v24, v44
	v_mul_f32_e32 v41, 0x3e4ccccd, v40
	v_cmp_lt_f32_e32 vcc, 0, v40
	v_pk_fma_f32 v[14:15], v[38:39], v[42:43], v[14:15] op_sel_hi:[1,0,1]
	v_pk_fma_f32 v[12:13], v[48:49], v[42:43], v[12:13] op_sel:[0,1,0]
	v_cndmask_b32_e32 v40, v41, v40, vcc
	v_add_f32_e32 v41, v25, v45
	v_mul_f32_e32 v44, 0x3e4ccccd, v41
	v_cmp_lt_f32_e32 vcc, 0, v41
	v_fma_f32 v40, s16, v40, v58
	v_mul_f32_e32 v40, 0x3fb8aa3b, v40
	v_cndmask_b32_e32 v41, v44, v41, vcc
	v_fma_f32 v41, s16, v41, v58
	v_mul_f32_e32 v41, 0x3fb8aa3b, v41
	v_exp_f32_e32 v40, v40
	v_exp_f32_e32 v41, v41
	v_pk_fma_f32 v[10:11], v[46:47], v[42:43], v[10:11] op_sel:[0,1,0]
	v_pk_add_f32 v[72:73], v[72:73], v[42:43]
	v_pk_add_f32 v[38:39], v[40:41], -1.0 op_sel_hi:[1,0]
	s_nop 0
	v_pk_fma_f32 v[8:9], v[56:57], v[38:39], v[8:9] op_sel_hi:[1,0,1]
	v_pk_fma_f32 v[6:7], v[54:55], v[38:39], v[6:7] op_sel_hi:[1,0,1]
	v_pk_add_f32 v[70:71], v[70:71], v[38:39]
	v_pk_fma_f32 v[4:5], v[52:53], v[38:39], v[4:5] op_sel:[0,1,0]
	v_pk_fma_f32 v[2:3], v[50:51], v[38:39], v[2:3] op_sel:[0,1,0]
.LBB5_87:
	s_cmp_lt_i32 s48, 3
	s_cbranch_scc1 .LBB5_89
	s_waitcnt vmcnt(8)
	ds_write_b128 v1, v[26:29]
	s_waitcnt vmcnt(7)
	ds_write_b128 v1, v[30:33] offset:1024
	s_waitcnt vmcnt(6)
	ds_write_b128 v1, v[34:37] offset:2048
	ds_read2_b32 v[30:31], v96 offset1:12
	ds_read2_b32 v[32:33], v96 offset0:24 offset1:36
	ds_read2_b32 v[38:39], v96 offset0:192 offset1:204
	ds_read2_b32 v[40:41], v96 offset0:216 offset1:228
	v_add_u32_e32 v26, 0x400, v96
	v_add_u32_e32 v34, 0x800, v96
	ds_read2_b32 v[42:43], v26 offset0:128 offset1:140
	ds_read2_b32 v[46:47], v26 offset0:152 offset1:164
	ds_read2_b32 v[48:49], v34 offset0:64 offset1:76
	ds_read_b128 v[26:29], v80
	ds_read2_b32 v[50:51], v34 offset0:88 offset1:100
	ds_read_b128 v[34:37], v80 offset:1024
	s_waitcnt lgkmcnt(9)
	v_cvt_pk_bf16_f32 v30, v30, v31
	s_waitcnt lgkmcnt(8)
	v_cvt_pk_bf16_f32 v31, v32, v33
	s_waitcnt lgkmcnt(7)
	v_cvt_pk_bf16_f32 v32, v38, v39
	s_waitcnt lgkmcnt(6)
	v_cvt_pk_bf16_f32 v33, v40, v41
	s_waitcnt lgkmcnt(5)
	v_cvt_pk_bf16_f32 v38, v42, v43
	ds_read_b128 v[42:45], v80 offset:2048
	s_waitcnt lgkmcnt(3)
	v_mfma_f32_16x16x32_bf16 v[26:29], v[26:29], v[30:33], 0
	v_cvt_pk_bf16_f32 v39, v46, v47
	v_cvt_pk_bf16_f32 v40, v48, v49
	s_waitcnt lgkmcnt(2)
	v_cvt_pk_bf16_f32 v41, v50, v51
	s_waitcnt lgkmcnt(0)
	v_mfma_f32_16x16x32_bf16 v[42:45], v[42:45], v[30:33], 0
	ds_read_b128 v[46:49], v80 offset:4096
	ds_read_b128 v[50:53], v80 offset:6144
	v_mfma_f32_16x16x32_bf16 v[26:29], v[34:37], v[38:41], v[26:29]
	ds_read_b128 v[34:37], v80 offset:3072
	s_waitcnt lgkmcnt(0)
	v_mfma_f32_16x16x32_bf16 v[34:37], v[34:37], v[38:41], v[42:45]
	s_nop 2
	ds_read_b128 v[42:45], v80 offset:5120
	v_mfma_f32_16x16x32_bf16 v[46:49], v[46:49], v[30:33], 0
	s_waitcnt lgkmcnt(0)
	v_mfma_f32_16x16x32_bf16 v[42:45], v[42:45], v[38:41], v[46:49]
	s_nop 5
	ds_read_b128 v[46:49], v80 offset:10240
	ds_read_b128 v[54:57], v80 offset:7168
	ds_read_b128 v[58:61], v80 offset:11264
	v_mfma_f32_16x16x32_bf16 v[50:53], v[50:53], v[30:33], 0
	s_waitcnt lgkmcnt(2)
	v_mfma_f32_16x16x32_bf16 v[30:33], v[46:49], v[30:33], v[18:21]
	s_waitcnt lgkmcnt(0)
	v_mfma_f32_16x16x32_bf16 v[30:33], v[58:61], v[38:41], v[30:33]
	v_mfma_f32_16x16x32_bf16 v[38:41], v[54:57], v[38:41], v[50:53]
	s_nop 6
	v_add_f32_e32 v30, v22, v30
	v_mul_f32_e32 v46, 0x3e4ccccd, v30
	v_cmp_lt_f32_e32 vcc, 0, v30
	v_add_f32_e32 v31, v23, v31
	v_mul_f32_e32 v47, 0x3e4ccccd, v31
	v_cndmask_b32_e32 v30, v46, v30, vcc
	v_cmp_lt_f32_e32 vcc, 0, v31
	v_mov_b32_e32 v46, s49
	v_fma_f32 v30, s17, v30, v46
	v_cndmask_b32_e32 v31, v47, v31, vcc
	v_fma_f32 v31, s17, v31, v46
	v_mul_f32_e32 v30, 0x3fb8aa3b, v30
	v_mul_f32_e32 v31, 0x3fb8aa3b, v31
	v_exp_f32_e32 v30, v30
	v_exp_f32_e32 v31, v31
	s_nop 0
	v_pk_add_f32 v[30:31], v[30:31], -1.0 op_sel_hi:[1,0]
	s_nop 0
	v_pk_fma_f32 v[16:17], v[28:29], v[30:31], v[16:17] op_sel_hi:[1,0,1]
	v_add_f32_e32 v28, v24, v32
	v_mul_f32_e32 v29, 0x3e4ccccd, v28
	v_cmp_lt_f32_e32 vcc, 0, v28
	v_pk_fma_f32 v[14:15], v[26:27], v[30:31], v[14:15] op_sel_hi:[1,0,1]
	v_pk_fma_f32 v[12:13], v[36:37], v[30:31], v[12:13] op_sel:[0,1,0]
	v_cndmask_b32_e32 v28, v29, v28, vcc
	v_add_f32_e32 v29, v25, v33
	v_mul_f32_e32 v32, 0x3e4ccccd, v29
	v_cmp_lt_f32_e32 vcc, 0, v29
	v_fma_f32 v28, s17, v28, v46
	v_mul_f32_e32 v28, 0x3fb8aa3b, v28
	v_cndmask_b32_e32 v29, v32, v29, vcc
	v_fmac_f32_e32 v46, s17, v29
	v_mul_f32_e32 v29, 0x3fb8aa3b, v46
	v_exp_f32_e32 v28, v28
	v_exp_f32_e32 v29, v29
	v_pk_fma_f32 v[10:11], v[34:35], v[30:31], v[10:11] op_sel:[0,1,0]
	v_pk_add_f32 v[72:73], v[72:73], v[30:31]
	v_pk_add_f32 v[26:27], v[28:29], -1.0 op_sel_hi:[1,0]
	s_nop 0
	v_pk_fma_f32 v[8:9], v[44:45], v[26:27], v[8:9] op_sel_hi:[1,0,1]
	v_pk_fma_f32 v[6:7], v[42:43], v[26:27], v[6:7] op_sel_hi:[1,0,1]
	v_pk_add_f32 v[70:71], v[70:71], v[26:27]
	v_pk_fma_f32 v[4:5], v[40:41], v[26:27], v[4:5] op_sel:[0,1,0]
	v_pk_fma_f32 v[2:3], v[38:39], v[26:27], v[2:3] op_sel:[0,1,0]
	s_cmp_lt_i32 s48, 4
	s_cbranch_scc1 .LBB5_92
	s_branch .LBB5_90

.LBB5_92:
	v_lshlrev_b32_e32 v1, 2, v131
	v_or_b32_e32 v18, 0x23d00, v1
	v_or_b32_e32 v22, 0x23d40, v1
	ds_read_b128 v[18:21], v18
	ds_read_b128 v[22:25], v22
	s_waitcnt vmcnt(8)
	v_rcp_f32_e32 v26, v72
	v_rcp_f32_e32 v28, v73
	s_waitcnt lgkmcnt(1)
	v_pk_fma_f32 v[14:15], v[26:27], v[14:15], v[18:19] op_sel_hi:[0,1,1]
	s_waitcnt lgkmcnt(0)
	v_pk_fma_f32 v[10:11], v[28:29], v[10:11], v[22:23] op_sel_hi:[0,1,1]
	v_pk_add_f32 v[120:121], v[14:15], v[88:89]
	v_pk_fma_f32 v[14:15], v[26:27], v[16:17], v[20:21] op_sel_hi:[0,1,1]
	v_pk_add_f32 v[118:119], v[10:11], v[86:87]
	v_or_b32_e32 v10, 0x23d80, v1
	v_pk_add_f32 v[122:123], v[14:15], v[90:91]
	v_pk_fma_f32 v[14:15], v[28:29], v[12:13], v[24:25] op_sel_hi:[0,1,1]
	ds_read_b128 v[10:13], v10
	v_rcp_f32_e32 v18, v70
	v_or_b32_e32 v1, 0x23dc0, v1
	v_pk_add_f32 v[124:125], v[14:15], v[82:83]
	ds_read_b128 v[14:17], v1
	s_waitcnt lgkmcnt(1)
	v_pk_fma_f32 v[6:7], v[18:19], v[6:7], v[10:11] op_sel_hi:[0,1,1]
	v_rcp_f32_e32 v10, v71
	v_pk_add_f32 v[116:117], v[6:7], v[66:67]
	v_pk_fma_f32 v[6:7], v[18:19], v[8:9], v[12:13] op_sel_hi:[0,1,1]
	v_pk_add_f32 v[114:115], v[6:7], v[68:69]
	s_waitcnt lgkmcnt(0)
	v_pk_fma_f32 v[2:3], v[10:11], v[2:3], v[14:15] op_sel_hi:[0,1,1]
	v_pk_add_f32 v[110:111], v[2:3], v[94:95]
	v_pk_fma_f32 v[2:3], v[10:11], v[4:5], v[16:17] op_sel_hi:[0,1,1]
	v_pk_add_f32 v[112:113], v[2:3], v[92:93]
	v_mul_f32_e32 v3, v130, v120
	v_mul_f32_e32 v2, v120, v3
	v_mul_f32_e32 v5, v130, v121
	v_pk_add_f32 v[2:3], v[2:3], 0 op_sel_hi:[1,0]
	v_mul_f32_e32 v4, v121, v5
	v_pk_add_f32 v[2:3], v[2:3], v[4:5]
	v_mul_f32_e32 v5, v130, v122
	v_mul_f32_e32 v4, v122, v5
	v_pk_add_f32 v[2:3], v[2:3], v[4:5]
	v_mul_f32_e32 v5, v130, v123
	v_mul_f32_e32 v4, v123, v5
	v_pk_add_f32 v[2:3], v[2:3], v[4:5]
	v_mul_f32_e32 v5, v130, v118
	v_mul_f32_e32 v4, v118, v5
	v_pk_add_f32 v[2:3], v[2:3], v[4:5]
	v_mul_f32_e32 v5, v130, v119
	v_mul_f32_e32 v4, v119, v5
	v_mul_f32_e32 v7, v130, v124
	v_mul_f32_e32 v6, v124, v7
	v_mul_f32_e32 v9, v130, v125
	v_pk_add_f32 v[2:3], v[2:3], v[4:5]
	v_mul_f32_e32 v8, v125, v9
	v_mul_f32_e32 v11, v130, v116
	v_pk_add_f32 v[2:3], v[2:3], v[6:7]
	v_mul_f32_e32 v10, v116, v11
	v_mul_f32_e32 v13, v130, v117
	v_pk_add_f32 v[2:3], v[2:3], v[8:9]
	v_mul_f32_e32 v12, v117, v13
	v_mul_f32_e32 v15, v130, v114
	v_pk_add_f32 v[2:3], v[2:3], v[10:11]
	v_mul_f32_e32 v14, v114, v15
	v_mul_f32_e32 v17, v130, v115
	v_pk_add_f32 v[2:3], v[2:3], v[12:13]
	v_mul_f32_e32 v16, v115, v17
	v_mul_f32_e32 v19, v130, v110
	v_pk_add_f32 v[2:3], v[2:3], v[14:15]
	v_mul_f32_e32 v18, v110, v19
	v_mul_f32_e32 v21, v130, v111
	v_pk_add_f32 v[2:3], v[2:3], v[16:17]
	v_mul_f32_e32 v20, v111, v21
	v_mul_f32_e32 v23, v130, v112
	v_pk_add_f32 v[2:3], v[2:3], v[18:19]
	v_mul_f32_e32 v22, v112, v23
	v_pk_add_f32 v[2:3], v[2:3], v[20:21]
	v_mul_f32_e32 v5, v130, v113
	v_pk_add_f32 v[2:3], v[2:3], v[22:23]
	v_mul_f32_e32 v4, v113, v5
	v_pk_add_f32 v[70:71], v[2:3], v[4:5]
.LBB5_93:
	s_mul_hi_i32 s7, s37, 0x300
	s_mul_i32 s6, s37, 0x300
	s_lshl_b64 s[14:15], s[6:7], 2
	s_add_u32 s6, s28, s14
	s_addc_u32 s7, s29, s15
	s_add_u32 s8, s30, s14
	s_addc_u32 s9, s31, s15
	s_movk_i32 s6, 0x3000
	v_add_co_u32_e32 v26, vcc, s6, v84
	v_or_b32_e32 v1, 0x800, v0
	s_nop 0
	v_addc_co_u32_e32 v27, vcc, 0, v85, vcc
	v_add_co_u32_e32 v28, vcc, 0x5000, v84
	s_movk_i32 s6, 0xb00
	s_nop 0
	v_addc_co_u32_e32 v29, vcc, 0, v85, vcc
	global_load_dwordx4 v[30:33], v[26:27], off
	global_load_dwordx4 v[34:37], v[28:29], off offset:2048
	v_cmp_gt_u32_e64 s[12:13], s6, v1
	s_and_saveexec_b64 s[6:7], s[12:13]
	s_cbranch_execz .LBB5_95
	v_lshlrev_b32_e32 v1, 4, v1
	global_load_dwordx4 v[26:29], v1, s[42:43]

.LBB5_104:
	ds_write_b128 v78, v[38:41] offset:43008
	s_or_b64 exec, exec, s[12:13]
	s_and_b64 vcc, exec, s[0:1]
	v_lshl_add_u32 v81, v128, 4, s46
	s_cbranch_vccnz .LBB5_107
	v_cndmask_b32_e64 v1, v79, v129, s[2:3]
	ds_write_b128 v81, v[136:139]
	ds_write_b128 v81, v[140:143] offset:1024
	ds_write_b128 v81, v[144:147] offset:2048
	v_lshl_add_u32 v1, v1, 2, s46
	ds_read_b32 v70, v1
	ds_read_b32 v71, v1 offset:48
	ds_read_b32 v72, v1 offset:96
	ds_read_b32 v73, v1 offset:144
	ds_read_b32 v74, v1 offset:768
	ds_read_b32 v75, v1 offset:816
	ds_read_b32 v76, v1 offset:864
	ds_read_b32 v77, v1 offset:912
	ds_read_b32 v96, v1 offset:1536
	ds_read_b32 v97, v1 offset:1584
	ds_read_b32 v152, v1 offset:1632
	ds_read_b32 v153, v1 offset:1680
	ds_read_b32 v90, v1 offset:2304
	ds_read_b32 v91, v1 offset:2352
	ds_read_b32 v92, v1 offset:2400
	ds_read_b32 v93, v1 offset:2448
	ds_write_b128 v81, v[148:151]
	ds_write_b128 v81, v[156:159] offset:1024
	ds_write_b128 v81, v[160:163] offset:2048
	ds_read_b32 v102, v1
	ds_read_b32 v103, v1 offset:48
	ds_read_b32 v104, v1 offset:96
	ds_read_b32 v105, v1 offset:144
	ds_read_b32 v106, v1 offset:768
	ds_read_b32 v107, v1 offset:816
	ds_read_b32 v108, v1 offset:864
	ds_read_b32 v109, v1 offset:912
	ds_read_b32 v86, v1 offset:1536
	ds_read_b32 v87, v1 offset:1584
	ds_read_b32 v88, v1 offset:1632
	ds_read_b32 v89, v1 offset:1680
	ds_read_b32 v98, v1 offset:2304
	ds_read_b32 v99, v1 offset:2352
	ds_read_b32 v100, v1 offset:2400
	ds_read_b32 v101, v1 offset:2448

.Lmy_inact93:
	s_waitcnt vmcnt(2)
	s_branch .LBB5_93
